# stick-breaking attention task setup: all 16 diagonal-tile K/V loads issued before waiting for the 8 Q loads (vmcnt(16) instead of a second load round trip); on top of c4
# speedup vs baseline: 1.0048x; 1.0048x over previous
.LBB0_452:
	s_or_b64 exec, exec, s[10:11]
	v_readfirstlane_b32 s10, v0
	s_cmpk_gt_i32 s10, 0x7ff
	s_cselect_b64 s[30:31], -1, 0
	s_and_b64 vcc, exec, s[30:31]
	s_cbranch_vccnz .LBB0_447
	s_lshl_b32 s14, s10, 1
	s_and_b32 s47, s10, 0x780
	s_lshl_b32 s11, s10, 5
	s_add_i32 s10, s14, s46
	s_and_b32 s56, s11, 0xfe0
	s_and_b32 s57, s10, 0xfffff000
	s_or_b32 s15, s57, s56
	s_lshl_b32 s10, s47, 1
	s_add_u32 s10, s50, s10
	s_addc_u32 s11, s51, 0
	v_add_u32_e32 v32, s15, v174
	v_mov_b64_e32 v[24:25], s[10:11]
	v_add_u32_e32 v34, s15, v175
	v_add_u32_e32 v36, s15, v176
	v_add_u32_e32 v38, s15, v177
	v_add_u32_e32 v40, s15, v178
	v_add_u32_e32 v41, s15, v179
	v_mad_i64_i32 v[0:1], s[12:13], v32, s3, v[24:25]
	v_mad_i64_i32 v[2:3], s[12:13], v34, s3, v[24:25]
	v_mad_i64_i32 v[8:9], s[12:13], v36, s3, v[24:25]
	v_mad_i64_i32 v[10:11], s[12:13], v38, s3, v[24:25]
	v_mad_i64_i32 v[16:17], s[12:13], v40, s3, v[24:25]
	v_mad_i64_i32 v[18:19], s[12:13], v41, s3, v[24:25]
	v_lshl_add_u64 v[0:1], v[0:1], 0, v[160:161]
	v_lshl_add_u64 v[4:5], v[2:3], 0, v[160:161]
	v_lshl_add_u64 v[8:9], v[8:9], 0, v[160:161]
	v_lshl_add_u64 v[12:13], v[10:11], 0, v[160:161]
	v_lshl_add_u64 v[16:17], v[16:17], 0, v[160:161]
	v_lshl_add_u64 v[20:21], v[18:19], 0, v[160:161]
	global_load_dwordx4 v[0:3], v[0:1], off
	s_nop 0
	global_load_dwordx4 v[4:7], v[4:5], off
	s_nop 0
	global_load_dwordx4 v[8:11], v[8:9], off
	s_nop 0
	global_load_dwordx4 v[12:15], v[12:13], off
	s_nop 0
	global_load_dwordx4 v[16:19], v[16:17], off
	s_nop 0
	global_load_dwordx4 v[20:23], v[20:21], off
	v_mov_b32_e32 v147, v161
	v_lshl_add_u64 v[148:149], s[10:11], 0, v[146:147]
	s_mov_b64 s[98:99], 0x2000
	v_lshl_add_u64 v[216:217], v[148:149], 0, s[98:99]
	v_mad_i64_i32 v[32:33], s[10:11], v32, s3, v[148:149]
	v_add_co_u32_e32 v32, vcc, s93, v32
	v_mad_i64_i32 v[34:35], s[10:11], v34, s3, v[148:149]
	s_nop 0
	v_addc_co_u32_e32 v33, vcc, 0, v33, vcc
	v_add_co_u32_e32 v34, vcc, s93, v34
	v_mad_i64_i32 v[36:37], s[10:11], v36, s3, v[148:149]
	s_nop 0
	v_addc_co_u32_e32 v35, vcc, 0, v35, vcc
	v_add_u32_e32 v42, s15, v180
	v_add_u32_e32 v43, s15, v181
	v_add_co_u32_e32 v36, vcc, s93, v36
	v_mad_i64_i32 v[26:27], s[12:13], v42, s3, v[24:25]
	v_mad_i64_i32 v[24:25], s[12:13], v43, s3, v[24:25]
	v_mad_i64_i32 v[38:39], s[10:11], v38, s3, v[148:149]
	v_addc_co_u32_e32 v37, vcc, 0, v37, vcc
	v_lshl_add_u64 v[26:27], v[26:27], 0, v[160:161]
	v_lshl_add_u64 v[28:29], v[24:25], 0, v[160:161]
	v_add_co_u32_e32 v38, vcc, s93, v38
	global_load_dwordx4 v[24:27], v[26:27], off
	s_nop 0
	global_load_dwordx4 v[28:31], v[28:29], off
	v_addc_co_u32_e32 v39, vcc, 0, v39, vcc
	global_load_dwordx4 v[80:83], v[32:33], off offset:-4096
	global_load_dwordx4 v[84:87], v[32:33], off
	global_load_dwordx4 v[88:91], v[34:35], off offset:-4096
	global_load_dwordx4 v[92:95], v[34:35], off
	global_load_dwordx4 v[96:99], v[36:37], off offset:-4096
	global_load_dwordx4 v[100:103], v[36:37], off
	global_load_dwordx4 v[104:107], v[38:39], off offset:-4096
	global_load_dwordx4 v[108:111], v[38:39], off
	v_mad_i64_i32 v[32:33], s[10:11], v40, s3, v[216:217]
	v_mad_i64_i32 v[34:35], s[10:11], v41, s3, v[216:217]
	v_mad_i64_i32 v[44:45], s[10:11], v42, s3, v[216:217]
	v_mad_i64_i32 v[46:47], s[10:11], v43, s3, v[216:217]
	global_load_dwordx4 v[112:115], v[32:33], off offset:-4096
	global_load_dwordx4 v[116:119], v[32:33], off
	global_load_dwordx4 v[120:123], v[34:35], off offset:-4096
	global_load_dwordx4 v[124:127], v[34:35], off
	global_load_dwordx4 v[128:131], v[44:45], off offset:-4096
	global_load_dwordx4 v[132:135], v[44:45], off
	global_load_dwordx4 v[136:139], v[46:47], off offset:-4096
	global_load_dwordx4 v[140:143], v[46:47], off
	v_mov_b32_e32 v48, 0
	s_mov_b32 s58, 0
	v_mov_b32_e32 v205, 1.0
	v_mov_b32_e32 v49, v48
	v_mov_b32_e32 v50, v48
	v_mov_b32_e32 v51, v48
	v_mov_b32_e32 v52, v48
	v_mov_b32_e32 v53, v48
	v_mov_b32_e32 v54, v48
	v_mov_b32_e32 v55, v48
	v_mov_b32_e32 v56, v48
	v_mov_b32_e32 v57, v48
	v_mov_b32_e32 v58, v48
	v_mov_b32_e32 v59, v48
	v_mov_b32_e32 v60, v48
	v_mov_b32_e32 v61, v48
	v_mov_b32_e32 v62, v48
	s_add_i32 s10, s43, s14
	s_and_b32 s10, s10, 0xfffff000
	s_or_b32 s10, s56, s10
	s_waitcnt vmcnt(16)
	ds_write_b128 v190, v[0:3] offset:8192
	ds_write_b128 v191, v[4:7] offset:8192
	ds_write_b128 v192, v[8:11] offset:8192
	ds_write_b128 v193, v[12:15] offset:8192
	ds_write_b128 v194, v[16:19] offset:8192
	ds_write_b128 v195, v[20:23] offset:8192
	ds_write_b128 v196, v[24:27] offset:8192
	ds_write_b128 v197, v[28:31] offset:8192
	v_add_u32_e32 v147, s10, v182
	v_add_u32_e32 v198, s10, v183
	v_add_u32_e32 v199, s10, v184
	v_add_u32_e32 v200, s10, v185
	v_add_u32_e32 v201, s10, v186
	v_add_u32_e32 v202, s10, v187
	v_add_u32_e32 v203, s10, v188
	v_add_u32_e32 v204, s10, v189
	v_mov_b32_e32 v63, v48
	v_mov_b32_e32 v32, v48
	v_mov_b32_e32 v33, v48
	v_mov_b32_e32 v34, v48
	v_mov_b32_e32 v35, v48
	v_mov_b32_e32 v36, v48
	v_mov_b32_e32 v37, v48
	v_mov_b32_e32 v38, v48
	v_mov_b32_e32 v39, v48
	v_mov_b32_e32 v40, v48
	v_mov_b32_e32 v41, v48
	v_mov_b32_e32 v42, v48
	v_mov_b32_e32 v43, v48
	v_mov_b32_e32 v44, v48
	v_mov_b32_e32 v45, v48
	v_mov_b32_e32 v46, v48
	v_mov_b32_e32 v47, v48
	v_mov_b32_e32 v16, v48
	v_mov_b32_e32 v17, v48
	v_mov_b32_e32 v18, v48
	v_mov_b32_e32 v19, v48
	v_mov_b32_e32 v20, v48
	v_mov_b32_e32 v21, v48
	v_mov_b32_e32 v22, v48
	v_mov_b32_e32 v23, v48
	v_mov_b32_e32 v24, v48
	v_mov_b32_e32 v25, v48
	v_mov_b32_e32 v26, v48
	v_mov_b32_e32 v27, v48
	v_mov_b32_e32 v28, v48
	v_mov_b32_e32 v29, v48
	v_mov_b32_e32 v30, v48
	v_mov_b32_e32 v31, v48
	v_mov_b32_e32 v0, v48
	v_mov_b32_e32 v1, v48
	v_mov_b32_e32 v2, v48
	v_mov_b32_e32 v3, v48
	v_mov_b32_e32 v4, v48
	v_mov_b32_e32 v5, v48
	v_mov_b32_e32 v6, v48
	v_mov_b32_e32 v7, v48
	v_mov_b32_e32 v8, v48
	v_mov_b32_e32 v9, v48
	v_mov_b32_e32 v10, v48
	v_mov_b32_e32 v11, v48
	v_mov_b32_e32 v12, v48
	v_mov_b32_e32 v13, v48
	v_mov_b32_e32 v14, v48
	v_mov_b32_e32 v15, v48
	s_branch .LBB0_455
